# P6c requests the second half of the z row at the row top; P0 x f32-to-bf16 stream keeps four chunks (8 loads) in flight per iteration
# speedup vs baseline: 1.0545x; 1.0024x over previous
; __device__ __forceinline__ unsigned pk2(float lo, float hi) { return pkbf(lo, hi); }
; __device__ __forceinline__ void cvt_bf16_stream(const float* __restrict__ src, bf16* __restrict__ dst, size_t nchunks, size_t gt, size_t GT) {
;     for (size_t c = gt; c < nchunks; c += GT) { const f4 a = ((const f4*)src)[2 * c], b = ((const f4*)src)[2 * c + 1];
;         u4 o; o.x = pk2(a.x, a.y); o.y = pk2(a.z, a.w); o.z = pk2(b.x, b.y); o.w = pk2(b.z, b.w); ((u4*)dst)[c] = o; }
; }
.LBB0_86:
	s_mov_b32 s14, 4
.Lp0e_loop:
	v_lshl_add_u64 v[16:17], v[4:5], 0, s[12:13]
	v_lshl_add_u64 v[18:19], v[16:17], 0, s[12:13]
	v_lshl_add_u64 v[20:21], v[18:19], 0, s[12:13]
	global_load_dwordx4 v[8:11], v[4:5], off offset:-16
	global_load_dwordx4 v[12:15], v[4:5], off
	global_load_dwordx4 v[24:27], v[16:17], off offset:-16
	global_load_dwordx4 v[28:31], v[16:17], off
	global_load_dwordx4 v[32:35], v[18:19], off offset:-16
	global_load_dwordx4 v[36:39], v[18:19], off
	global_load_dwordx4 v[40:43], v[20:21], off offset:-16
	global_load_dwordx4 v[44:47], v[20:21], off
	v_lshl_add_u64 v[4:5], v[20:21], 0, s[12:13]
	v_lshl_add_u64 v[48:49], v[2:3], 0, s[8:9]
	v_lshl_add_u64 v[50:51], v[48:49], 0, s[8:9]
	v_lshl_add_u64 v[52:53], v[50:51], 0, s[8:9]
	s_waitcnt vmcnt(6)
	v_cvt_pk_bf16_f32 v8, v8, v9
	v_cvt_pk_bf16_f32 v9, v10, v11
	v_cvt_pk_bf16_f32 v10, v12, v13
	v_cvt_pk_bf16_f32 v11, v14, v15
	global_store_dwordx4 v[2:3], v[8:11], off
	s_waitcnt vmcnt(5)
	v_cvt_pk_bf16_f32 v24, v24, v25
	v_cvt_pk_bf16_f32 v25, v26, v27
	v_cvt_pk_bf16_f32 v26, v28, v29
	v_cvt_pk_bf16_f32 v27, v30, v31
	global_store_dwordx4 v[48:49], v[24:27], off
	s_waitcnt vmcnt(4)
	v_cvt_pk_bf16_f32 v32, v32, v33
	v_cvt_pk_bf16_f32 v33, v34, v35
	v_cvt_pk_bf16_f32 v34, v36, v37
	v_cvt_pk_bf16_f32 v35, v38, v39
	global_store_dwordx4 v[50:51], v[32:35], off
	s_waitcnt vmcnt(3)
	v_cvt_pk_bf16_f32 v40, v40, v41
	v_cvt_pk_bf16_f32 v41, v42, v43
	v_cvt_pk_bf16_f32 v42, v44, v45
	v_cvt_pk_bf16_f32 v43, v46, v47
	global_store_dwordx4 v[52:53], v[40:43], off
	v_lshl_add_u64 v[2:3], v[52:53], 0, s[8:9]
	s_sub_u32 s14, s14, 1
	s_cmp_lg_u32 s14, 0
	s_cbranch_scc1 .Lp0e_loop

; __device__ __forceinline__ void row_peer_reduce(const Params& P, unsigned char* ws, int l, int rowi, int lane, float* __restrict__ xout) {
;     const size_t n = (size_t)rowi; const bf16* Z = (const bf16*)(ws + WS_Z); const unsigned char* PARTQ = ws + WS_PART; const float* PSCL = (const float*)(ws + WS_PSCL);
;     const f2 st = *(const f2*)((const float*)(ws + WS_X1) + 2 * n);
;     const float* g1 = P.in[16] + (size_t)l * D; const float* b1 = P.in[17] + (size_t)l * D;
;     float acc[32];
; #pragma unroll
;     for (int j = 0; j < 2; ++j)
; #pragma unroll
;         for (int q = 0; q < 4; ++q) { const int col = 1024 * j + 16 * lane + 4 * q; const u2 zw = *(const u2*)(Z + n * D + col); const f4 a = mk_f4(__uint_as_float(zw.x << 16), __uint_as_float(zw.x & 0xffff0000u), __uint_as_float(zw.y << 16), __uint_as_float(zw.y & 0xffff0000u)), gg = *(const f4*)(g1 + col), bb = *(const f4*)(b1 + col);
;             acc[16 * j + 4 * q] = ALPHA * ((a.x - st.x) * st.y * gg.x + bb.x); acc[16 * j + 4 * q + 1] = ALPHA * ((a.y - st.x) * st.y * gg.y + bb.y);
;             acc[16 * j + 4 * q + 2] = ALPHA * ((a.z - st.x) * st.y * gg.z + bb.z); acc[16 * j + 4 * q + 3] = ALPHA * ((a.w - st.x) * st.y * gg.w + bb.w); }
; #pragma unroll 4
;     for (int xb_ = 0; xb_ < 8; ++xb_) { const u4 a = *(const u4*)(PARTQ + ((size_t)xb_ * NTOK + ((n + 5u * (unsigned)xb_) & (size_t)(NTOK - 1))) * 1024u + (unsigned)(16 * lane)); const float psc = PSCL[(size_t)xb_ * NTOK + n];
.LBB0_1592:
	s_add_u32 s26, s92, 0x5b000000
	s_addc_u32 s27, s93, 0
	s_add_u32 s28, s92, 0x64000000
	s_addc_u32 s29, s93, 0
	s_and_b32 s22, s6, 0x1fff
	s_lshl_b32 s22, s22, 10
	v_add_u32_e32 v144, s22, v32
	global_load_dwordx4 v[104:107], v144, s[26:27]
	s_lshl_b32 s23, s6, 2
	v_mov_b32_e32 v176, s23
	global_load_dword v136, v176, s[28:29]
	s_add_i32 s22, s6, 5
	s_and_b32 s22, s22, 0x1fff
	s_lshl_b32 s22, s22, 10
	s_add_i32 s22, s22, 0x800000
	v_add_u32_e32 v145, s22, v32
	global_load_dwordx4 v[108:111], v145, s[26:27]
	s_add_i32 s23, s6, 0x2000
	s_lshl_b32 s23, s23, 2
	v_mov_b32_e32 v177, s23
	global_load_dword v137, v177, s[28:29]
	s_add_i32 s22, s6, 10
	s_and_b32 s22, s22, 0x1fff
	s_lshl_b32 s22, s22, 10
	s_add_i32 s22, s22, 0x1000000
	v_add_u32_e32 v146, s22, v32
	global_load_dwordx4 v[112:115], v146, s[26:27]
	s_add_i32 s23, s6, 0x4000
	s_lshl_b32 s23, s23, 2
	v_mov_b32_e32 v178, s23
	global_load_dword v138, v178, s[28:29]
	s_add_i32 s22, s6, 15
	s_and_b32 s22, s22, 0x1fff
	s_lshl_b32 s22, s22, 10
	s_add_i32 s22, s22, 0x1800000
	v_add_u32_e32 v147, s22, v32
	global_load_dwordx4 v[116:119], v147, s[26:27]
	s_add_i32 s23, s6, 0x6000
	s_lshl_b32 s23, s23, 2
	v_mov_b32_e32 v179, s23
	global_load_dword v139, v179, s[28:29]
	s_add_i32 s22, s6, 20
	s_and_b32 s22, s22, 0x1fff
	s_lshl_b32 s22, s22, 10
	s_add_i32 s22, s22, 0x2000000
	v_add_u32_e32 v148, s22, v32
	global_load_dwordx4 v[120:123], v148, s[26:27]
	s_add_i32 s23, s6, 0x8000
	s_lshl_b32 s23, s23, 2
	v_mov_b32_e32 v180, s23
	global_load_dword v140, v180, s[28:29]
	s_add_i32 s22, s6, 25
	s_and_b32 s22, s22, 0x1fff
	s_lshl_b32 s22, s22, 10
	s_add_i32 s22, s22, 0x2800000
	v_add_u32_e32 v149, s22, v32
	global_load_dwordx4 v[124:127], v149, s[26:27]
	s_add_i32 s23, s6, 0xa000
	s_lshl_b32 s23, s23, 2
	v_mov_b32_e32 v181, s23
	global_load_dword v141, v181, s[28:29]
	s_add_i32 s22, s6, 30
	s_and_b32 s22, s22, 0x1fff
	s_lshl_b32 s22, s22, 10
	s_add_i32 s22, s22, 0x3000000
	v_add_u32_e32 v150, s22, v32
	global_load_dwordx4 v[128:131], v150, s[26:27]
	s_add_i32 s23, s6, 0xc000
	s_lshl_b32 s23, s23, 2
	v_mov_b32_e32 v182, s23
	global_load_dword v142, v182, s[28:29]
	s_add_i32 s22, s6, 35
	s_and_b32 s22, s22, 0x1fff
	s_lshl_b32 s22, s22, 10
	s_add_i32 s22, s22, 0x3800000
	v_add_u32_e32 v151, s22, v32
	global_load_dwordx4 v[132:135], v151, s[26:27]
	s_add_i32 s23, s6, 0xe000
	s_lshl_b32 s23, s23, 2
	v_mov_b32_e32 v183, s23
	global_load_dword v143, v183, s[28:29]
	s_ashr_i32 s7, s6, 31
	s_lshl_b64 s[4:5], s[6:7], 3
	s_add_u32 s4, s38, s4
	s_addc_u32 s5, s39, s5
	global_load_dwordx2 v[74:75], v80, s[4:5]
	s_lshl_b64 s[12:13], s[6:7], 12
	v_lshl_add_u64 v[4:5], v[52:53], 0, s[12:13]
	global_load_dwordx4 v[0:3], v[4:5], off offset:16
	global_load_dwordx4 v[6:9], v[4:5], off
	global_load_dwordx4 v[184:187], v[4:5], off offset:2064
	global_load_dwordx4 v[188:191], v[4:5], off offset:2048
	global_load_dwordx4 v[10:13], v[34:35], off offset:48
	global_load_dwordx4 v[14:17], v[34:35], off offset:32
	global_load_dwordx4 v[18:21], v[34:35], off offset:16
	global_load_dwordx4 v[22:25], v[34:35], off
	global_load_dwordx4 v[26:29], v[36:37], off offset:48
	global_load_dwordx4 v[64:67], v[36:37], off offset:32
	global_load_dwordx4 v[60:63], v[36:37], off offset:16
	global_load_dwordx4 v[56:59], v[36:37], off
	s_mov_b32 s4, 0x3fd744fd
	s_mov_b64 s[14:15], 0x4000
	s_mov_b64 s[16:17], 0x2000
	s_mov_b64 s[18:19], 0
	s_mov_b32 s47, s46
	s_mov_b32 s48, s45
	s_mov_b32 s49, s44
	s_mov_b32 s50, s43
	s_mov_b64 s[34:35], 0
	s_waitcnt vmcnt(0)
; __device__ __forceinline__ void row_peer_reduce(const Params& P, unsigned char* ws, int l, int rowi, int lane, float* __restrict__ xout) {
;     ...
;     for (int j = 0; j < 2; ++j)
; #pragma unroll
;         for (int q = 0; q < 4; ++q) { const int col = 1024 * j + 16 * lane + 4 * q; const u2 zw = *(const u2*)(Z + n * D + col); const f4 a = mk_f4(__uint_as_float(zw.x << 16), __uint_as_float(zw.x & 0xffff0000u), __uint_as_float(zw.y << 16), __uint_as_float(zw.y & 0xffff0000u)), gg = *(const f4*)(g1 + col), bb = *(const f4*)(b1 + col);
;             acc[16 * j + 4 * q] = ALPHA * ((a.x - st.x) * st.y * gg.x + bb.x); acc[16 * j + 4 * q + 1] = ALPHA * ((a.y - st.x) * st.y * gg.y + bb.y);
;             acc[16 * j + 4 * q + 2] = ALPHA * ((a.z - st.x) * st.y * gg.z + bb.z); acc[16 * j + 4 * q + 3] = ALPHA * ((a.w - st.x) * st.y * gg.w + bb.w); }
	v_lshlrev_b32_e32 v30, 16, v6
	v_and_b32_e32 v31, 0xffff0000, v6
	v_lshlrev_b32_e32 v6, 16, v7
	v_and_b32_e32 v7, 0xffff0000, v7
	v_pk_add_f32 v[6:7], v[6:7], v[74:75] op_sel_hi:[1,0] neg_lo:[0,1] neg_hi:[0,1]
	s_nop 0
	v_pk_mul_f32 v[6:7], v[74:75], v[6:7] op_sel:[1,0]
	v_pk_add_f32 v[30:31], v[30:31], v[74:75] op_sel_hi:[1,0] neg_lo:[0,1] neg_hi:[0,1]
	v_pk_fma_f32 v[6:7], v[24:25], v[6:7], v[58:59]
	v_pk_mul_f32 v[30:31], v[74:75], v[30:31] op_sel:[1,0]
	v_pk_mul_f32 v[58:59], v[6:7], s[4:5] op_sel_hi:[1,0]
	v_lshlrev_b32_e32 v6, 16, v8
	v_and_b32_e32 v7, 0xffff0000, v8
	v_pk_add_f32 v[6:7], v[6:7], v[74:75] op_sel_hi:[1,0] neg_lo:[0,1] neg_hi:[0,1]
	v_pk_fma_f32 v[22:23], v[22:23], v[30:31], v[56:57]
	v_pk_mul_f32 v[6:7], v[74:75], v[6:7] op_sel:[1,0]
	v_pk_mul_f32 v[56:57], v[22:23], s[4:5] op_sel_hi:[1,0]
	v_pk_fma_f32 v[6:7], v[18:19], v[6:7], v[60:61]
	s_nop 0
	v_pk_mul_f32 v[60:61], v[6:7], s[4:5] op_sel_hi:[1,0]
	v_lshlrev_b32_e32 v6, 16, v9
	v_and_b32_e32 v7, 0xffff0000, v9
	v_pk_add_f32 v[6:7], v[6:7], v[74:75] op_sel_hi:[1,0] neg_lo:[0,1] neg_hi:[0,1]
	s_nop 0
	v_pk_mul_f32 v[6:7], v[74:75], v[6:7] op_sel:[1,0]
	s_nop 0
	v_pk_fma_f32 v[6:7], v[20:21], v[6:7], v[62:63]
	s_nop 0
	v_pk_mul_f32 v[62:63], v[6:7], s[4:5] op_sel_hi:[1,0]
	v_lshlrev_b32_e32 v6, 16, v0
	v_and_b32_e32 v7, 0xffff0000, v0
	v_lshlrev_b32_e32 v0, 16, v1
	v_and_b32_e32 v1, 0xffff0000, v1
	v_pk_add_f32 v[0:1], v[0:1], v[74:75] op_sel_hi:[1,0] neg_lo:[0,1] neg_hi:[0,1]
	v_pk_add_f32 v[6:7], v[6:7], v[74:75] op_sel_hi:[1,0] neg_lo:[0,1] neg_hi:[0,1]
	v_pk_mul_f32 v[0:1], v[74:75], v[0:1] op_sel:[1,0]
	v_pk_mul_f32 v[6:7], v[74:75], v[6:7] op_sel:[1,0]
	v_pk_fma_f32 v[0:1], v[16:17], v[0:1], v[66:67]
	v_pk_fma_f32 v[6:7], v[14:15], v[6:7], v[64:65]
	v_pk_mul_f32 v[66:67], v[0:1], s[4:5] op_sel_hi:[1,0]
	v_lshlrev_b32_e32 v0, 16, v2
	v_and_b32_e32 v1, 0xffff0000, v2
	v_pk_add_f32 v[0:1], v[0:1], v[74:75] op_sel_hi:[1,0] neg_lo:[0,1] neg_hi:[0,1]
	v_pk_mul_f32 v[64:65], v[6:7], s[4:5] op_sel_hi:[1,0]
	v_pk_mul_f32 v[0:1], v[74:75], v[0:1] op_sel:[1,0]
	s_nop 0
	v_pk_fma_f32 v[0:1], v[10:11], v[0:1], v[26:27]
	s_nop 0
	v_pk_mul_f32 v[68:69], v[0:1], s[4:5] op_sel_hi:[1,0]
	v_lshlrev_b32_e32 v0, 16, v3
	v_and_b32_e32 v1, 0xffff0000, v3
	v_pk_add_f32 v[0:1], v[0:1], v[74:75] op_sel_hi:[1,0] neg_lo:[0,1] neg_hi:[0,1]
	s_nop 0
	v_pk_mul_f32 v[0:1], v[74:75], v[0:1] op_sel:[1,0]
	s_nop 0
	v_pk_fma_f32 v[0:1], v[12:13], v[0:1], v[28:29]
	s_nop 0
	v_pk_mul_f32 v[70:71], v[0:1], s[4:5] op_sel_hi:[1,0]
	v_mov_b64_e32 v[0:1], v[184:185]
	v_mov_b64_e32 v[2:3], v[186:187]
	v_mov_b64_e32 v[28:29], v[188:189]
	v_mov_b64_e32 v[30:31], v[190:191]
	s_nop 0
	global_load_dwordx4 v[4:7], v[38:39], off offset:48
	global_load_dwordx4 v[12:15], v[38:39], off offset:32
	global_load_dwordx4 v[20:23], v[38:39], off offset:16
	global_load_dwordx4 v[82:85], v[38:39], off
	global_load_dwordx4 v[8:11], v[40:41], off offset:48
	global_load_dwordx4 v[16:19], v[40:41], off offset:32
	global_load_dwordx4 v[24:27], v[40:41], off offset:16
	global_load_dwordx4 v[86:89], v[40:41], off
	s_waitcnt vmcnt(8)
	v_lshlrev_b32_e32 v72, 16, v28
	v_and_b32_e32 v73, 0xffff0000, v28
	v_pk_add_f32 v[72:73], v[72:73], v[74:75] op_sel_hi:[1,0] neg_lo:[0,1] neg_hi:[0,1]
	v_lshlrev_b32_e32 v28, 16, v29
	v_pk_mul_f32 v[72:73], v[74:75], v[72:73] op_sel:[1,0]
	v_and_b32_e32 v29, 0xffff0000, v29
	v_pk_add_f32 v[28:29], v[28:29], v[74:75] op_sel_hi:[1,0] neg_lo:[0,1] neg_hi:[0,1]
	s_waitcnt vmcnt(0)
	v_pk_fma_f32 v[72:73], v[82:83], v[72:73], v[86:87]
	v_lshlrev_b32_e32 v82, 16, v30
	v_and_b32_e32 v83, 0xffff0000, v30
	v_pk_add_f32 v[82:83], v[82:83], v[74:75] op_sel_hi:[1,0] neg_lo:[0,1] neg_hi:[0,1]
	v_pk_mul_f32 v[28:29], v[74:75], v[28:29] op_sel:[1,0]
	v_pk_mul_f32 v[82:83], v[74:75], v[82:83] op_sel:[1,0]
	v_pk_fma_f32 v[28:29], v[84:85], v[28:29], v[88:89]
	v_pk_fma_f32 v[20:21], v[20:21], v[82:83], v[24:25]
	v_lshlrev_b32_e32 v24, 16, v31
	v_and_b32_e32 v25, 0xffff0000, v31
	v_pk_add_f32 v[24:25], v[24:25], v[74:75] op_sel_hi:[1,0] neg_lo:[0,1] neg_hi:[0,1]
	v_pk_mul_f32 v[72:73], v[72:73], s[4:5] op_sel_hi:[1,0]
	v_pk_mul_f32 v[24:25], v[74:75], v[24:25] op_sel:[1,0]
	v_pk_mul_f32 v[28:29], v[28:29], s[4:5] op_sel_hi:[1,0]
	v_pk_fma_f32 v[22:23], v[22:23], v[24:25], v[26:27]
	v_lshlrev_b32_e32 v24, 16, v0
	v_and_b32_e32 v25, 0xffff0000, v0
	v_lshlrev_b32_e32 v0, 16, v1
	v_and_b32_e32 v1, 0xffff0000, v1
	v_pk_add_f32 v[0:1], v[0:1], v[74:75] op_sel_hi:[1,0] neg_lo:[0,1] neg_hi:[0,1]
	v_pk_add_f32 v[24:25], v[24:25], v[74:75] op_sel_hi:[1,0] neg_lo:[0,1] neg_hi:[0,1]
	v_pk_mul_f32 v[0:1], v[74:75], v[0:1] op_sel:[1,0]
	v_pk_mul_f32 v[24:25], v[74:75], v[24:25] op_sel:[1,0]
	v_pk_fma_f32 v[0:1], v[14:15], v[0:1], v[18:19]
	v_lshlrev_b32_e32 v14, 16, v2
	v_and_b32_e32 v15, 0xffff0000, v2
	v_lshlrev_b32_e32 v2, 16, v3
	v_and_b32_e32 v3, 0xffff0000, v3
	v_pk_add_f32 v[14:15], v[14:15], v[74:75] op_sel_hi:[1,0] neg_lo:[0,1] neg_hi:[0,1]
	v_pk_add_f32 v[2:3], v[2:3], v[74:75] op_sel_hi:[1,0] neg_lo:[0,1] neg_hi:[0,1]
	v_pk_mul_f32 v[14:15], v[74:75], v[14:15] op_sel:[1,0]
	v_pk_mul_f32 v[2:3], v[74:75], v[2:3] op_sel:[1,0]
	v_pk_fma_f32 v[12:13], v[12:13], v[24:25], v[16:17]
	v_pk_fma_f32 v[4:5], v[4:5], v[14:15], v[8:9]
	v_pk_fma_f32 v[2:3], v[6:7], v[2:3], v[10:11]
	v_pk_mul_f32 v[20:21], v[20:21], s[4:5] op_sel_hi:[1,0]
	v_pk_mul_f32 v[22:23], v[22:23], s[4:5] op_sel_hi:[1,0]
	v_pk_mul_f32 v[12:13], v[12:13], s[4:5] op_sel_hi:[1,0]
	v_pk_mul_f32 v[0:1], v[0:1], s[4:5] op_sel_hi:[1,0]
	v_pk_mul_f32 v[4:5], v[4:5], s[4:5] op_sel_hi:[1,0]
	v_pk_mul_f32 v[2:3], v[2:3], s[4:5] op_sel_hi:[1,0]
	s_mov_b64 s[4:5], 0x6000
